# attention QK block: 8 K-fragment ds_reads issued up front with counted lgkmcnt
# speedup vs baseline: 1.0735x; 1.0735x over previous
.LBB0_705:
	s_movk_i32 s10, 0x6a00
	v_add3_u32 v217, v201, v202, s10
	s_add_i32 s10, s29, 6
	s_cmp_lt_i32 s10, s28
	s_cselect_b32 s14, s10, s22
	s_cmp_lt_i32 s14, s35
	s_cselect_b64 s[24:25], -1, 0
	s_and_b64 s[10:11], s[24:25], exec
	s_cselect_b32 s10, 0, s35
	s_cselect_b32 s11, s20, s23
	s_sub_i32 s10, s14, s10
	s_lshl_b32 s14, s10, 6
	s_add_i32 s10, s14, s11
	v_add_u32_e32 v112, s10, v197
	s_movk_i32 s10, 0x4a00
	v_mad_i64_i32 v[112:113], s[10:11], v112, s10, v[204:205]
	s_add_i32 s10, s29, 5
	s_cmp_lt_i32 s10, s28
	s_cselect_b32 s10, s10, s22
	s_cmp_lt_i32 s10, s35
	s_cselect_b32 s11, 0, s35
	s_cselect_b32 s15, s33, 0x1000
	s_sub_i32 s10, s10, s11
	s_lshl_b32 s10, s10, 6
	s_add_i32 s10, s10, s15
	s_waitcnt vmcnt(7)
	ds_write_b128 v199, v[164:167]
	s_waitcnt vmcnt(6)
	ds_write2_b64 v217, v[160:161], v[162:163] offset1:1
	s_ashr_i32 s11, s10, 31
	v_lshl_add_u64 v[114:115], s[10:11], 1, v[206:207]
	global_load_dwordx4 v[164:167], v[112:113], off
	global_load_dwordx4 v[160:163], v[114:115], off
	s_add_i32 s15, s29, 1
	s_cmp_lt_i32 s15, s28
	s_cselect_b64 s[18:19], -1, 0
	s_cmp_ge_i32 s15, s35
	s_cselect_b64 s[10:11], -1, 0
	s_or_b64 s[10:11], s[0:1], s[10:11]
	s_cmp_ge_i32 s15, s21
	s_cselect_b64 s[26:27], -1, 0
	s_cmp_lt_i32 s29, s2
	s_cselect_b64 s[30:31], -1, 0
	s_and_b64 s[26:27], s[26:27], s[30:31]
	s_or_b64 s[10:11], s[10:11], s[26:27]
	s_and_b64 s[26:27], s[18:19], s[10:11]
	v_cndmask_b32_e64 v112, 0, 1, s[26:27]
	v_cmp_ne_u32_e64 s[10:11], 1, v112
	s_andn2_b64 vcc, exec, s[26:27]
	v_add_u32_e32 v216, v210, v208
	s_cbranch_vccnz .LBB0_707
	ds_read_b128 v[112:115], v216 offset:17920
	ds_read_b128 v[116:119], v216 offset:22528
	ds_read_b128 v[120:123], v216 offset:17952
	ds_read_b128 v[124:127], v216 offset:22560
	ds_read_b128 v[128:131], v216 offset:17984
	ds_read_b128 v[132:135], v216 offset:22592
	ds_read_b128 v[136:139], v216 offset:18016
	ds_read_b128 v[140:143], v216 offset:22624
	s_waitcnt lgkmcnt(7)
	v_mfma_f32_32x32x16_bf16 v[80:95], v[112:115], v[144:147], v[32:47]
	s_waitcnt lgkmcnt(6)
	v_mfma_f32_32x32x16_bf16 v[96:111], v[116:119], v[144:147], v[32:47]
	s_waitcnt lgkmcnt(5)
	v_mfma_f32_32x32x16_bf16 v[80:95], v[120:123], v[148:151], v[80:95]
	s_waitcnt lgkmcnt(4)
	v_mfma_f32_32x32x16_bf16 v[96:111], v[124:127], v[148:151], v[96:111]
	s_waitcnt lgkmcnt(3)
	v_mfma_f32_32x32x16_bf16 v[80:95], v[128:131], v[152:155], v[80:95]
	s_waitcnt lgkmcnt(2)
	v_mfma_f32_32x32x16_bf16 v[96:111], v[132:135], v[152:155], v[96:111]
	s_waitcnt lgkmcnt(1)
	v_mfma_f32_32x32x16_bf16 v[80:95], v[136:139], v[156:159], v[80:95]
	s_waitcnt lgkmcnt(0)
	v_mfma_f32_32x32x16_bf16 v[96:111], v[140:143], v[156:159], v[96:111]

.LBB0_754:
	s_add_i32 s10, s29, 7
	s_cmp_lt_i32 s10, s28
	s_cselect_b32 s26, s10, s22
	s_cmp_lt_i32 s26, s35
	s_cselect_b64 s[30:31], -1, 0
	s_and_b64 s[10:11], s[30:31], exec
	s_cselect_b32 s10, 0, s35
	s_cselect_b32 s11, s20, s23
	s_sub_i32 s10, s26, s10
	s_lshl_b32 s40, s10, 6
	s_add_i32 s10, s40, s11
	v_add_u32_e32 v112, s10, v197
	s_movk_i32 s10, 0x4a00
	v_mad_i64_i32 v[112:113], s[10:11], v112, s10, v[204:205]
	s_and_b64 s[10:11], s[24:25], exec
	s_cselect_b32 s10, s33, 0x1000
	s_add_i32 s10, s14, s10
	s_waitcnt lgkmcnt(0)
	s_barrier
	s_waitcnt vmcnt(7)
	ds_write_b128 v199, v[168:171] offset:17920
	s_waitcnt vmcnt(6)
	ds_write2_b64 v203, v[172:173], v[174:175] offset1:1
	s_ashr_i32 s11, s10, 31
	v_lshl_add_u64 v[114:115], s[10:11], 1, v[206:207]
	global_load_dwordx4 v[168:171], v[112:113], off
	global_load_dwordx4 v[172:175], v[114:115], off
	s_add_i32 s14, s29, 2
	s_cmp_lt_i32 s14, s28
	s_cselect_b64 s[26:27], -1, 0
	s_cmp_ge_i32 s14, s35
	s_cselect_b64 s[10:11], -1, 0
	s_or_b64 s[10:11], s[0:1], s[10:11]
	s_cmp_ge_i32 s14, s21
	s_cselect_b64 s[24:25], -1, 0
	s_cmp_lt_i32 s15, s2
	s_cselect_b64 vcc, -1, 0
	s_and_b64 s[24:25], s[24:25], vcc
	s_or_b64 s[10:11], s[10:11], s[24:25]
	s_and_b64 s[24:25], s[26:27], s[10:11]
	v_cndmask_b32_e64 v112, 0, 1, s[24:25]
	v_cmp_ne_u32_e64 s[10:11], 1, v112
	s_andn2_b64 vcc, exec, s[24:25]
	s_cbranch_vccnz .LBB0_756
	ds_read_b128 v[112:115], v216
	ds_read_b128 v[116:119], v216 offset:4608
	ds_read_b128 v[120:123], v216 offset:32
	ds_read_b128 v[124:127], v216 offset:4640
	ds_read_b128 v[128:131], v216 offset:64
	ds_read_b128 v[132:135], v216 offset:4672
	ds_read_b128 v[136:139], v216 offset:96
	ds_read_b128 v[140:143], v216 offset:4704
	s_waitcnt lgkmcnt(7)
	v_mfma_f32_32x32x16_bf16 v[48:63], v[112:115], v[144:147], v[32:47]
	s_waitcnt lgkmcnt(6)
	v_mfma_f32_32x32x16_bf16 v[64:79], v[116:119], v[144:147], v[32:47]
	s_waitcnt lgkmcnt(5)
	v_mfma_f32_32x32x16_bf16 v[48:63], v[120:123], v[148:151], v[48:63]
	s_waitcnt lgkmcnt(4)
	v_mfma_f32_32x32x16_bf16 v[64:79], v[124:127], v[148:151], v[64:79]
	s_waitcnt lgkmcnt(3)
	v_mfma_f32_32x32x16_bf16 v[48:63], v[128:131], v[152:155], v[48:63]
	s_waitcnt lgkmcnt(2)
	v_mfma_f32_32x32x16_bf16 v[64:79], v[132:135], v[152:155], v[64:79]
	s_waitcnt lgkmcnt(1)
	v_mfma_f32_32x32x16_bf16 v[48:63], v[136:139], v[156:159], v[48:63]
	s_waitcnt lgkmcnt(0)
	v_mfma_f32_32x32x16_bf16 v[64:79], v[140:143], v[156:159], v[64:79]

.LBB0_803:
	s_add_i32 s10, s29, 8
	s_cmp_lt_i32 s10, s28
	s_cselect_b32 s15, s10, s22
	s_cmp_lt_i32 s15, s35
	s_cselect_b64 s[24:25], -1, 0
	s_and_b64 s[10:11], s[24:25], exec
	s_cselect_b32 s10, 0, s35
	s_cselect_b32 s11, s20, s23
	s_sub_i32 s10, s15, s10
	s_lshl_b32 s34, s10, 6
	s_add_i32 s10, s34, s11
	v_add_u32_e32 v112, s10, v197
	s_movk_i32 s10, 0x4a00
	v_mad_i64_i32 v[112:113], s[10:11], v112, s10, v[204:205]
	s_and_b64 s[10:11], s[30:31], exec
	s_cselect_b32 s10, s33, 0x1000
	s_add_i32 s10, s40, s10
	s_waitcnt lgkmcnt(0)
	s_barrier
	s_waitcnt vmcnt(7)
	ds_write_b128 v199, v[176:179]
	s_waitcnt vmcnt(6)
	ds_write2_b64 v217, v[180:181], v[182:183] offset1:1
	s_ashr_i32 s11, s10, 31
	v_lshl_add_u64 v[114:115], s[10:11], 1, v[206:207]
	global_load_dwordx4 v[176:179], v[112:113], off
	global_load_dwordx4 v[180:183], v[114:115], off
	s_add_i32 s30, s29, 3
	s_cmp_lt_i32 s30, s28
	s_cselect_b64 s[18:19], -1, 0
	s_cmp_ge_i32 s30, s35
	s_cselect_b64 s[10:11], -1, 0
	s_or_b64 s[10:11], s[0:1], s[10:11]
	s_cmp_ge_i32 s30, s21
	s_cselect_b64 s[40:41], -1, 0
	s_cmp_lt_i32 s14, s2
	s_cselect_b64 vcc, -1, 0
	s_and_b64 s[40:41], s[40:41], vcc
	s_or_b64 s[10:11], s[10:11], s[40:41]
	s_and_b64 s[40:41], s[18:19], s[10:11]
	v_cndmask_b32_e64 v112, 0, 1, s[40:41]
	v_cmp_ne_u32_e64 s[10:11], 1, v112
	s_andn2_b64 vcc, exec, s[40:41]
	s_cbranch_vccnz .LBB0_805
	ds_read_b128 v[112:115], v216 offset:17920
	ds_read_b128 v[116:119], v216 offset:22528
	ds_read_b128 v[120:123], v216 offset:17952
	ds_read_b128 v[124:127], v216 offset:22560
	ds_read_b128 v[128:131], v216 offset:17984
	ds_read_b128 v[132:135], v216 offset:22592
	ds_read_b128 v[136:139], v216 offset:18016
	ds_read_b128 v[140:143], v216 offset:22624
	s_waitcnt lgkmcnt(7)
	v_mfma_f32_32x32x16_bf16 v[80:95], v[112:115], v[144:147], v[32:47]
	s_waitcnt lgkmcnt(6)
	v_mfma_f32_32x32x16_bf16 v[96:111], v[116:119], v[144:147], v[32:47]
	s_waitcnt lgkmcnt(5)
	v_mfma_f32_32x32x16_bf16 v[80:95], v[120:123], v[148:151], v[80:95]
	s_waitcnt lgkmcnt(4)
	v_mfma_f32_32x32x16_bf16 v[96:111], v[124:127], v[148:151], v[96:111]
	s_waitcnt lgkmcnt(3)
	v_mfma_f32_32x32x16_bf16 v[80:95], v[128:131], v[152:155], v[80:95]
	s_waitcnt lgkmcnt(2)
	v_mfma_f32_32x32x16_bf16 v[96:111], v[132:135], v[152:155], v[96:111]
	s_waitcnt lgkmcnt(1)
	v_mfma_f32_32x32x16_bf16 v[80:95], v[136:139], v[156:159], v[80:95]
	s_waitcnt lgkmcnt(0)
	v_mfma_f32_32x32x16_bf16 v[96:111], v[140:143], v[156:159], v[96:111]

.LBB0_852:
	s_add_i32 s10, s29, 9
	s_cmp_lt_i32 s10, s28
	s_cselect_b32 s10, s10, s22
	s_cmp_lt_i32 s10, s35
	s_cselect_b32 s11, 0, s35
	s_cselect_b32 s14, s20, s23
	s_sub_i32 s10, s10, s11
	s_lshl_b32 s10, s10, 6
	s_add_i32 s10, s10, s14
	v_add_u32_e32 v112, s10, v197
	s_movk_i32 s10, 0x4a00
	v_mad_i64_i32 v[112:113], s[10:11], v112, s10, v[204:205]
	s_and_b64 s[10:11], s[24:25], exec
	s_cselect_b32 s10, s33, 0x1000
	s_add_i32 s10, s34, s10
	s_waitcnt lgkmcnt(0)
	s_barrier
	s_waitcnt vmcnt(7)
	ds_write_b128 v199, v[184:187] offset:17920
	s_waitcnt vmcnt(6)
	ds_write2_b64 v203, v[188:189], v[190:191] offset1:1
	s_ashr_i32 s11, s10, 31
	v_lshl_add_u64 v[114:115], s[10:11], 1, v[206:207]
	global_load_dwordx4 v[184:187], v[112:113], off
	global_load_dwordx4 v[188:191], v[114:115], off
	s_add_i32 s24, s29, 4
	s_cmp_lt_i32 s29, s35
	s_cselect_b64 s[10:11], -1, 0
	s_cmp_ge_i32 s24, s35
	s_cselect_b64 s[14:15], -1, 0
	s_or_b64 s[14:15], s[0:1], s[14:15]
	s_cmp_ge_i32 s24, s21
	s_cselect_b64 s[26:27], -1, 0
	s_cmp_lt_i32 s30, s2
	s_cselect_b64 s[40:41], -1, 0
	s_and_b64 s[26:27], s[26:27], s[40:41]
	s_or_b64 s[14:15], s[14:15], s[26:27]
	s_and_b64 s[14:15], s[10:11], s[14:15]
	v_cndmask_b32_e64 v112, 0, 1, s[14:15]
	v_cmp_ne_u32_e64 s[10:11], 1, v112
	s_andn2_b64 vcc, exec, s[14:15]
	s_cbranch_vccnz .LBB0_854
	ds_read_b128 v[112:115], v216
	ds_read_b128 v[116:119], v216 offset:4608
	ds_read_b128 v[120:123], v216 offset:32
	ds_read_b128 v[124:127], v216 offset:4640
	ds_read_b128 v[128:131], v216 offset:64
	ds_read_b128 v[132:135], v216 offset:4672
	ds_read_b128 v[136:139], v216 offset:96
	ds_read_b128 v[140:143], v216 offset:4704
	s_waitcnt lgkmcnt(7)
	v_mfma_f32_32x32x16_bf16 v[48:63], v[112:115], v[144:147], v[32:47]
	s_waitcnt lgkmcnt(6)
	v_mfma_f32_32x32x16_bf16 v[64:79], v[116:119], v[144:147], v[32:47]
	s_waitcnt lgkmcnt(5)
	v_mfma_f32_32x32x16_bf16 v[48:63], v[120:123], v[148:151], v[48:63]
	s_waitcnt lgkmcnt(4)
	v_mfma_f32_32x32x16_bf16 v[64:79], v[124:127], v[148:151], v[64:79]
	s_waitcnt lgkmcnt(3)
	v_mfma_f32_32x32x16_bf16 v[48:63], v[128:131], v[152:155], v[48:63]
	s_waitcnt lgkmcnt(2)
	v_mfma_f32_32x32x16_bf16 v[64:79], v[132:135], v[152:155], v[64:79]
	s_waitcnt lgkmcnt(1)
	v_mfma_f32_32x32x16_bf16 v[48:63], v[136:139], v[156:159], v[48:63]
	s_waitcnt lgkmcnt(0)
	v_mfma_f32_32x32x16_bf16 v[64:79], v[140:143], v[156:159], v[64:79]
